# dilated attention: 2x s_nop 15 spacer between softmax end and the first PV MFMA in both halves of the item loop
# speedup vs baseline: 1.0214x; 1.0214x over previous
.LBB0_297:
	v_lshlrev_b32_e32 v64, 1, v182
	v_and_b32_e32 v64, 8, v64
	v_and_or_b32 v68, v182, -16, v64
	v_lshrrev_b32_e32 v65, 2, v192
	v_bfe_u32 v66, v185, 3, 2
	v_lshrrev_b32_e32 v69, 1, v182
	v_lshrrev_b32_e32 v70, 2, v68
	v_lshlrev_b32_e32 v67, 4, v192
	v_or_b32_e32 v70, v70, v65
	v_and_or_b32 v69, v69, 4, v66
	v_and_b32_e32 v67, 48, v67
	v_lshlrev_b32_e32 v69, 6, v69
	v_lshl_add_u32 v70, v70, 9, s80
	v_add3_u32 v70, v70, v69, v67
	s_waitcnt vmcnt(7)
	ds_write_b128 v70, v[60:63]
	v_add_u32_e32 v60, 8, v182
	v_and_or_b32 v61, v60, s60, v64
	v_lshrrev_b32_e32 v60, 1, v60
	v_lshrrev_b32_e32 v61, 2, v61
	v_or_b32_e32 v61, v61, v65
	v_and_or_b32 v60, v60, 4, v66
	v_lshlrev_b32_e32 v60, 6, v60
	v_lshl_add_u32 v61, v61, 9, s80
	v_add3_u32 v60, v61, v60, v67
	s_waitcnt vmcnt(6)
	ds_write_b128 v60, v[56:59]
	v_add_u32_e32 v56, 16, v68
	v_lshrrev_b32_e32 v56, 2, v56
	v_or_b32_e32 v56, v56, v65
	v_lshl_add_u32 v56, v56, 9, s80
	v_add3_u32 v56, v56, v69, v67
	s_waitcnt vmcnt(5)
	ds_write_b128 v56, v[52:55]
	v_add_u32_e32 v52, 24, v182
	v_and_or_b32 v53, v52, s60, v64
	v_lshrrev_b32_e32 v52, 1, v52
	v_lshrrev_b32_e32 v53, 2, v53
	v_or_b32_e32 v53, v53, v65
	v_and_or_b32 v52, v52, 4, v66
	v_lshlrev_b32_e32 v52, 6, v52
	v_lshl_add_u32 v53, v53, 9, s80
	v_add3_u32 v52, v53, v52, v67
	s_waitcnt vmcnt(4)
	ds_write_b128 v52, v[48:51]
	v_add_u32_e32 v48, 32, v68
	v_lshrrev_b32_e32 v48, 2, v48
	v_or_b32_e32 v48, v48, v65
	v_lshl_add_u32 v48, v48, 9, s80
	v_add3_u32 v48, v48, v69, v67
	s_waitcnt vmcnt(3)
	ds_write_b128 v48, v[44:47]
	v_add_u32_e32 v44, 40, v182
	v_and_or_b32 v45, v44, s60, v64
	v_lshrrev_b32_e32 v44, 1, v44
	v_lshrrev_b32_e32 v45, 2, v45
	v_or_b32_e32 v45, v45, v65
	v_and_or_b32 v44, v44, 4, v66
	v_lshlrev_b32_e32 v44, 6, v44
	v_lshl_add_u32 v45, v45, 9, s80
	v_add3_u32 v44, v45, v44, v67
	s_waitcnt vmcnt(2)
	ds_write_b128 v44, v[40:43]
	v_add_u32_e32 v40, 48, v68
	v_lshrrev_b32_e32 v40, 2, v40
	v_or_b32_e32 v40, v40, v65
	v_lshl_add_u32 v40, v40, 9, s80
	v_add3_u32 v40, v40, v69, v67
	s_waitcnt vmcnt(1)
	ds_write_b128 v40, v[36:39]
	v_add_u32_e32 v36, 56, v182
	s_mov_b32 s25, s17
	v_and_or_b32 v37, v36, s60, v64
	s_lshl_b64 s[4:5], s[24:25], s82
	v_lshrrev_b32_e32 v36, 1, v36
	v_lshrrev_b32_e32 v37, 2, v37
	s_mulk_i32 s5, 0x1800
	s_mul_hi_u32 s16, s4, 0x1800
	s_add_i32 s41, s90, s94
	s_add_i32 s43, s73, s93
	s_add_i32 s31, s72, s91
	s_add_i32 s37, s97, s89
	s_add_i32 s35, s96, s88
	s_add_i32 s39, s95, s87
	v_or_b32_e32 v37, v37, v65
	v_and_or_b32 v36, v36, 4, v66
	s_add_i32 s5, s16, s5
	s_mulk_i32 s4, 0x1800
	v_lshlrev_b32_e32 v36, 6, v36
	v_lshl_add_u32 v37, v37, 9, s80
	s_add_u32 s44, s7, s4
	v_add3_u32 v36, v37, v36, v67
	s_addc_u32 s45, s85, s5
	s_waitcnt vmcnt(0)
	ds_write_b128 v36, v[32:35]
	v_lshl_add_u64 v[32:33], v[168:169], 1, s[44:45]
	v_lshl_add_u64 v[34:35], s[28:29], 1, v[32:33]
	global_load_dwordx4 v[64:67], v[32:33], off
	global_load_dwordx4 v[68:71], v[34:35], off
	v_lshl_add_u64 v[34:35], v[32:33], 0, s[40:41]
	global_load_dwordx4 v[72:75], v[34:35], off
	v_lshl_add_u64 v[34:35], v[32:33], 0, s[42:43]
	global_load_dwordx4 v[76:79], v[34:35], off
	v_lshl_add_u64 v[34:35], v[32:33], 0, s[30:31]
	global_load_dwordx4 v[80:83], v[34:35], off
	v_lshl_add_u64 v[34:35], v[32:33], 0, s[36:37]
	global_load_dwordx4 v[84:87], v[34:35], off
	v_lshl_add_u64 v[34:35], v[32:33], 0, s[34:35]
	v_lshl_add_u64 v[32:33], v[32:33], 0, s[38:39]
	global_load_dwordx4 v[88:91], v[34:35], off
	global_load_dwordx4 v[92:95], v[32:33], off
	s_waitcnt lgkmcnt(0)
	ds_read_b64_tr_b16 v[48:49], v189 offset:0
	ds_read_b64_tr_b16 v[50:51], v189 offset:0x400
	ds_read_b64_tr_b16 v[52:53], v189 offset:0x200
	ds_read_b64_tr_b16 v[54:55], v189 offset:0x600
	s_waitcnt lgkmcnt(0)
	s_nop 15
	s_nop 15
	s_nop 0
	v_mfma_f32_32x32x16_bf16 v[32:47], v[28:31], v[48:51], v[0:15]
	v_mfma_f32_32x32x16_bf16 v[0:15], v[28:31], v[52:55], v[0:15]
	ds_read_b64_tr_b16 v[28:29], v189 offset:0x800
	ds_read_b64_tr_b16 v[30:31], v189 offset:0xc00
	ds_read_b64_tr_b16 v[48:49], v189 offset:0xa00
	ds_read_b64_tr_b16 v[50:51], v189 offset:0xe00
	s_waitcnt lgkmcnt(0)
	s_nop 0
	v_mfma_f32_32x32x16_bf16 v[32:47], v[24:27], v[28:31], v[32:47]
	v_mfma_f32_32x32x16_bf16 v[0:15], v[24:27], v[48:51], v[0:15]
	ds_read_b64_tr_b16 v[24:25], v189 offset:0x1000
	ds_read_b64_tr_b16 v[26:27], v189 offset:0x1400
	ds_read_b64_tr_b16 v[28:29], v189 offset:0x1200
	ds_read_b64_tr_b16 v[30:31], v189 offset:0x1600
	s_waitcnt lgkmcnt(0)
	s_nop 0
	v_mfma_f32_32x32x16_bf16 v[32:47], v[20:23], v[24:27], v[32:47]
	v_mfma_f32_32x32x16_bf16 v[0:15], v[20:23], v[28:31], v[0:15]
	ds_read_b64_tr_b16 v[20:21], v189 offset:0x1800
	ds_read_b64_tr_b16 v[22:23], v189 offset:0x1c00
	ds_read_b64_tr_b16 v[24:25], v189 offset:0x1a00
	ds_read_b64_tr_b16 v[26:27], v189 offset:0x1e00
	s_waitcnt lgkmcnt(0)
	s_nop 0
	v_mfma_f32_32x32x16_bf16 v[32:47], v[16:19], v[20:23], v[32:47]
	v_mfma_f32_32x32x16_bf16 v[0:15], v[16:19], v[24:27], v[0:15]
	ds_read2_b32 v[16:17], v160 offset0:64 offset1:65
	ds_read2_b32 v[18:19], v160 offset0:66 offset1:67
	ds_read2_b32 v[20:21], v160 offset0:72 offset1:73
	ds_read2_b32 v[22:23], v160 offset0:74 offset1:75
	ds_read2_b32 v[24:25], v160 offset0:80 offset1:81
	ds_read2_b32 v[26:27], v160 offset0:82 offset1:83
	ds_read2_b32 v[28:29], v160 offset0:88 offset1:89
	ds_read2_b32 v[30:31], v160 offset0:90 offset1:91
	ds_read_b128 v[48:51], v161 offset:4096
	s_waitcnt lgkmcnt(0)
	v_mfma_f32_32x32x16_bf16 v[16:31], v[48:51], v[112:115], v[16:31]
	ds_read_b128 v[48:51], v162 offset:4096
	s_waitcnt lgkmcnt(0)
	v_mfma_f32_32x32x16_bf16 v[16:31], v[48:51], v[116:119], v[16:31]
	ds_read_b128 v[48:51], v163 offset:4096
	s_waitcnt lgkmcnt(0)
	v_mfma_f32_32x32x16_bf16 v[16:31], v[48:51], v[120:123], v[16:31]
	ds_read_b128 v[48:51], v164 offset:4096
	s_waitcnt lgkmcnt(0)
	v_mfma_f32_32x32x16_bf16 v[16:31], v[48:51], v[124:127], v[16:31]
	s_nop 11
	v_max_f32_e32 v48, v20, v20
	v_max_f32_e32 v49, v16, v16
	v_max_f32_e32 v48, v49, v48
	v_max_f32_e32 v49, v21, v21
	v_max_f32_e32 v50, v17, v17
	v_max_f32_e32 v49, v50, v49
	v_max_f32_e32 v50, v23, v23
	v_max_f32_e32 v51, v19, v19
	v_max_f32_e32 v50, v51, v50
	v_max3_f32 v51, v18, v22, v26
	v_max3_f32 v50, v50, v27, v31
	v_max3_f32 v48, v48, v24, v28
	v_max3_f32 v49, v49, v25, v29
	v_max3_f32 v50, v51, v30, v50
	v_max3_f32 v48, v48, v49, v50
	v_mov_b32_e32 v49, v48
	s_nop 1
	v_permlane32_swap_b32_e32 v48, v49
	v_max_f32_e32 v49, v49, v49
	v_max_f32_e32 v48, v48, v48
	v_max_f32_e32 v48, v48, v49
	v_add_f32_e32 v49, 0x461c4000, v48
	v_cmp_ge_f32_e32 vcc, s59, v49
	s_cmp_eq_u64 vcc, exec
	s_cbranch_scc0 .LBB0_338
	v_mov_b32_e32 v48, 1.0
	v_mov_b32_e32 v191, 0xc61c4000

.LBB0_312:
	s_waitcnt lgkmcnt(0)
	ds_read_b64_tr_b16 v[80:81], v189 offset:0
	ds_read_b64_tr_b16 v[82:83], v189 offset:0x400
	ds_read_b64_tr_b16 v[84:85], v189 offset:0x200
	ds_read_b64_tr_b16 v[86:87], v189 offset:0x600
	s_waitcnt lgkmcnt(0)
	s_nop 15
	s_nop 15
	s_nop 0
	v_mfma_f32_32x32x16_bf16 v[32:47], v[76:79], v[80:83], v[32:47]
	ds_read_b64_tr_b16 v[80:81], v189 offset:0x800
	ds_read_b64_tr_b16 v[82:83], v189 offset:0xc00
	ds_read_b64_tr_b16 v[88:89], v189 offset:0xa00
	ds_read_b64_tr_b16 v[90:91], v189 offset:0xe00
	s_waitcnt lgkmcnt(0)
	v_mfma_f32_32x32x16_bf16 v[0:15], v[76:79], v[84:87], v[0:15]
	v_mfma_f32_32x32x16_bf16 v[32:47], v[72:75], v[80:83], v[32:47]
	ds_read_b64_tr_b16 v[76:77], v189 offset:0x1000
	ds_read_b64_tr_b16 v[78:79], v189 offset:0x1400
	ds_read_b64_tr_b16 v[80:81], v189 offset:0x1200
	ds_read_b64_tr_b16 v[82:83], v189 offset:0x1600
	s_waitcnt lgkmcnt(0)
	v_mfma_f32_32x32x16_bf16 v[0:15], v[72:75], v[88:91], v[0:15]
	v_mfma_f32_32x32x16_bf16 v[32:47], v[68:71], v[76:79], v[32:47]
	ds_read_b64_tr_b16 v[72:73], v189 offset:0x1800
	ds_read_b64_tr_b16 v[74:75], v189 offset:0x1c00
	ds_read_b64_tr_b16 v[76:77], v189 offset:0x1a00
	ds_read_b64_tr_b16 v[78:79], v189 offset:0x1e00
	s_waitcnt lgkmcnt(0)
	v_mfma_f32_32x32x16_bf16 v[0:15], v[68:71], v[80:83], v[0:15]
	v_mfma_f32_32x32x16_bf16 v[32:47], v[64:67], v[72:75], v[32:47]
	v_mfma_f32_32x32x16_bf16 v[0:15], v[64:67], v[76:79], v[0:15]
	ds_read2_b32 v[64:65], v193 offset0:96 offset1:97
	ds_read2_b32 v[66:67], v193 offset0:98 offset1:99
	ds_read2_b32 v[68:69], v193 offset0:104 offset1:105
	ds_read2_b32 v[70:71], v193 offset0:106 offset1:107
	ds_read_b128 v[88:91], v194
	ds_read2_b32 v[72:73], v193 offset0:112 offset1:113
	ds_read2_b32 v[74:75], v193 offset0:114 offset1:115
	ds_read2_b32 v[76:77], v193 offset0:120 offset1:121
	ds_read2_b32 v[78:79], v193 offset0:122 offset1:123
	ds_read2_b32 v[80:81], v193 offset0:128 offset1:129
	ds_read2_b32 v[82:83], v193 offset0:130 offset1:131
	ds_read2_b32 v[84:85], v193 offset0:136 offset1:137
	ds_read2_b32 v[86:87], v193 offset0:138 offset1:139
	ds_read_b128 v[212:215], v194 offset:4096
	s_waitcnt lgkmcnt(5)
	v_mfma_f32_32x32x16_bf16 v[64:79], v[88:91], v[112:115], v[64:79]
	ds_read2_b32 v[88:89], v193 offset0:144 offset1:145
	ds_read2_b32 v[90:91], v193 offset0:146 offset1:147
	ds_read2_b32 v[92:93], v193 offset0:152 offset1:153
	ds_read2_b32 v[94:95], v193 offset0:154 offset1:155
	s_waitcnt lgkmcnt(0)
	v_mfma_f32_32x32x16_bf16 v[80:95], v[212:215], v[112:115], v[80:95]
	ds_read_b128 v[212:215], v195
	ds_read_b128 v[216:219], v195 offset:4096
	s_waitcnt lgkmcnt(1)
	v_mfma_f32_32x32x16_bf16 v[64:79], v[212:215], v[116:119], v[64:79]
	s_waitcnt lgkmcnt(0)
	v_mfma_f32_32x32x16_bf16 v[80:95], v[216:219], v[116:119], v[80:95]
	ds_read_b128 v[212:215], v196
	ds_read_b128 v[216:219], v196 offset:4096
	s_waitcnt lgkmcnt(1)
	v_mfma_f32_32x32x16_bf16 v[64:79], v[212:215], v[120:123], v[64:79]
	ds_read_b128 v[212:215], v197
	ds_read_b128 v[220:223], v197 offset:4096
	s_waitcnt lgkmcnt(2)
	v_mfma_f32_32x32x16_bf16 v[80:95], v[216:219], v[120:123], v[80:95]
	s_waitcnt lgkmcnt(1)
	v_mfma_f32_32x32x16_bf16 v[64:79], v[212:215], v[124:127], v[64:79]
	s_waitcnt lgkmcnt(0)
	v_mfma_f32_32x32x16_bf16 v[80:95], v[220:223], v[124:127], v[80:95]
	s_nop 9
	v_max_f32_e32 v192, v68, v68
	v_max_f32_e32 v212, v64, v64
	v_max_f32_e32 v192, v212, v192
	v_max_f32_e32 v212, v69, v69
	v_max_f32_e32 v213, v65, v65
	v_max_f32_e32 v212, v213, v212
	v_max_f32_e32 v213, v71, v71
	v_max_f32_e32 v214, v67, v67
	v_max_f32_e32 v213, v214, v213
	v_max3_f32 v214, v66, v70, v74
	v_max3_f32 v213, v213, v75, v79
	v_max3_f32 v192, v192, v72, v76
	v_max3_f32 v212, v212, v73, v77
	v_max3_f32 v214, v214, v78, v82
	v_max3_f32 v213, v213, v83, v87
	v_max3_f32 v192, v192, v80, v84
	v_max3_f32 v212, v212, v81, v85
	v_max3_f32 v214, v214, v86, v90
	v_max3_f32 v213, v213, v91, v95
	v_max3_f32 v192, v192, v88, v92
	v_max3_f32 v212, v212, v89, v93
	v_max3_f32 v213, v214, v94, v213
	v_max3_f32 v192, v192, v212, v213
	v_mov_b32_e32 v212, v192
	s_nop 1
	v_permlane32_swap_b32_e32 v192, v212
	v_max_f32_e32 v212, v212, v212
	v_max_f32_e32 v192, v192, v192
	v_max_f32_e32 v192, v192, v212
	v_sub_f32_e32 v212, v192, v191
	v_cmp_ge_f32_e32 vcc, s59, v212
	s_cmp_eq_u64 vcc, exec
	v_mov_b32_e32 v212, 1.0
	s_cbranch_scc0 .LBB0_336
